# baseline (speedup 1.0000x reference)
.LBB0_20:
	s_andn2_b64 vcc, exec, s[10:11]
	s_cbranch_vccnz .LBB0_33
	v_lshlrev_b32_e32 v216, 2, v216
	v_mov_b32_e32 v217, 0
	s_nop 1
	v_lshl_add_u64 v[2:3], s[26:27], 0, v[216:217]
	v_lshlrev_b32_e32 v216, 2, v221
	s_waitcnt vmcnt(7)
	v_lshl_add_u64 v[116:117], v[2:3], 0, v[216:217]
	v_lshlrev_b32_e32 v119, 12, v214
	s_and_saveexec_b64 s[10:11], s[6:7]
	s_xor_b64 s[56:57], exec, s[10:11]
	s_cbranch_execz .LBB0_27
	s_and_b32 s6, s2, 1
	s_lshl_b32 s3, s30, 20
	s_lshl_b32 s6, s6, 19
	s_or_b32 s3, s3, s6
	v_lshl_add_u32 v2, v219, 13, s3
	v_bfe_u32 v3, v0, 6, 2
	v_and_b32_e32 v4, 6, v222
	v_or3_b32 v118, v2, v119, v232
	v_mov_b32_e32 v2, 0
	s_mov_b32 s3, 0
	v_lshlrev_b32_e32 v119, 4, v218
	s_waitcnt vmcnt(6)
	v_lshlrev_b32_e32 v120, 10, v3
	v_lshlrev_b32_e32 v121, 10, v4
	s_mov_b64 s[58:59], 0x200
	s_mov_b32 s23, 0
	v_mov_b32_e32 v3, v2
	v_mov_b32_e32 v4, v2
	v_mov_b32_e32 v5, v2
	v_mov_b32_e32 v6, v2
	v_mov_b32_e32 v7, v2
	v_mov_b32_e32 v8, v2
	v_mov_b32_e32 v9, v2
	v_mov_b32_e32 v10, v2
	v_mov_b32_e32 v11, v2
	v_mov_b32_e32 v12, v2
	v_mov_b32_e32 v13, v2
	v_mov_b32_e32 v14, v2
	v_mov_b32_e32 v15, v2
	v_mov_b32_e32 v16, v2
	v_mov_b32_e32 v17, v2
	v_mov_b32_e32 v18, v2
	v_mov_b32_e32 v19, v2
	v_mov_b32_e32 v20, v2
	v_mov_b32_e32 v21, v2
	v_mov_b32_e32 v22, v2
	v_mov_b32_e32 v23, v2
	v_mov_b32_e32 v24, v2
	v_mov_b32_e32 v25, v2
	v_mov_b32_e32 v26, v2
	v_mov_b32_e32 v27, v2
	v_mov_b32_e32 v28, v2
	v_mov_b32_e32 v29, v2
	v_mov_b32_e32 v30, v2
	v_mov_b32_e32 v31, v2
	v_mov_b32_e32 v32, v2
	v_mov_b32_e32 v33, v2
	s_branch .LBB0_24

.LBB0_33:
	s_waitcnt vmcnt(15)
	v_lshl_add_u64 v[34:35], v[46:47], 2, s[48:49]
	v_add_co_u32_e32 v36, vcc, 0x2000, v34
	v_lshlrev_b32_e32 v1, 2, v231
	s_nop 0
	v_addc_co_u32_e32 v37, vcc, 0, v35, vcc
	s_waitcnt lgkmcnt(0)
	global_load_dword v104, v1, s[60:61]
	global_load_dword v100, v1, s[62:63]
	global_load_dwordx4 v[38:41], v[34:35], off
	s_nop 0
	global_load_dwordx4 v[34:37], v[36:37], off
	v_bfe_u32 v0, v0, 6, 2
	s_waitcnt vmcnt(17)
	v_and_b32_e32 v42, 6, v222
	v_lshl_or_b32 v0, v214, 4, v0
	v_mov_b32_e32 v43, 0x10000
	s_waitcnt vmcnt(15)
	v_lshl_or_b32 v103, v220, 3, v43
	v_lshlrev_b32_e32 v42, 1, v42
	v_mul_u32_u24_e32 v0, 0x110, v0
	v_cvt_pk_f16_f32 v2, v18, v2
	v_add3_u32 v18, v103, v42, v0
	v_cvt_pk_f16_f32 v0, v19, v3
	ds_write_b32 v18, v0 offset:1088
	v_cvt_pk_f16_f32 v0, v20, v4
	ds_write_b32 v18, v0 offset:2176
	v_cvt_pk_f16_f32 v0, v21, v5
	ds_write_b32 v18, v0 offset:3264
	v_cvt_pk_f16_f32 v0, v22, v6
	ds_write_b32 v18, v0 offset:8704
	v_cvt_pk_f16_f32 v0, v23, v7
	ds_write_b32 v18, v0 offset:9792
	v_cvt_pk_f16_f32 v0, v24, v8
	ds_write_b32 v18, v0 offset:10880
	v_cvt_pk_f16_f32 v0, v25, v9
	ds_write_b32 v18, v0 offset:11968
	v_cvt_pk_f16_f32 v0, v26, v10
	ds_write_b32 v18, v0 offset:17408
	v_cvt_pk_f16_f32 v0, v27, v11
	ds_write_b32 v18, v0 offset:18496
	v_cvt_pk_f16_f32 v0, v28, v12
	ds_write_b32 v18, v0 offset:19584
	v_cvt_pk_f16_f32 v0, v29, v13
	ds_write_b32 v18, v0 offset:20672
	v_cvt_pk_f16_f32 v0, v30, v14
	ds_write_b32 v18, v0 offset:26112
	v_cvt_pk_f16_f32 v0, v31, v15
	ds_write_b32 v18, v0 offset:27200
	v_cvt_pk_f16_f32 v0, v32, v16
	ds_write_b32 v18, v0 offset:28288
	v_mbcnt_lo_u32_b32 v0, -1, 0
	v_mbcnt_hi_u32_b32 v101, -1, v0
	ds_write_b32 v18, v2
	v_and_b32_e32 v2, 64, v101
	v_xor_b32_e32 v0, 32, v101
	v_add_u32_e32 v2, 64, v2
	v_cmp_lt_i32_e32 vcc, v0, v2
	s_load_dword s10, s[66:67], 0x0
	v_cndmask_b32_e32 v0, v101, v0, vcc
	v_lshlrev_b32_e32 v102, 2, v0
	ds_bpermute_b32 v0, v102, v217
	v_cmp_gt_u32_e32 vcc, 32, v218
	v_lshlrev_b32_e32 v1, 2, v220
	s_movk_i32 s6, 0x110
	v_cvt_pk_f16_f32 v2, v33, v17
	s_and_b64 s[12:13], s[4:5], vcc
	ds_write_b32 v18, v2 offset:29376
	s_and_saveexec_b64 s[0:1], s[12:13]
	s_cbranch_execz .LBB0_35
	s_waitcnt lgkmcnt(0)
	v_add_f32_e32 v0, v217, v0
	v_cvt_f16_f32_e32 v0, v0
	v_lshlrev_b32_e32 v2, 1, v1
	v_lshlrev_b32_e32 v3, 1, v219
	s_mov_b32 s7, 0x21000
	v_add3_u32 v2, v3, v2, s7
	ds_write_b16 v2, v0

.LBB0_37:
	s_or_b64 exec, exec, s[0:1]
	v_mov_b32_e32 v98, v97
	v_mov_b32_e32 v99, v97
	v_mov_b32_e32 v5, v97
	v_mov_b32_e32 v6, v97
	v_mov_b32_e32 v7, v97
	v_mov_b32_e32 v1, v97
	v_mov_b32_e32 v2, v97
	v_mov_b32_e32 v3, v97
	s_mov_b32 s0, 0x10000
	v_or_b32_e32 v8, 0x21000, v223
	v_mfma_f32_32x32x16_f16 v[32:47], v[96:99], v[0:3], 0
	v_mfma_f32_32x32x16_f16 v[16:31], v[4:7], v[0:3], 0
	v_or_b32_e32 v114, 0x21000, v223
	v_cmp_eq_u32_e64 s[0:1], 0, v225
	s_and_b64 vcc, vcc, s[0:1]
	ds_read_b128 v[8:11], v114
	ds_read_b128 v[12:15], v114 offset:32
	ds_read_b128 v[234:237], v114 offset:64
	ds_read_b128 v[238:241], v114 offset:96
	ds_read_b128 v[242:245], v114 offset:128
	ds_read_b128 v[106:109], v114 offset:160
	ds_read_b128 v[110:113], v114 offset:192
	s_waitcnt lgkmcnt(7)
	v_mfma_f32_32x32x16_f16 v[32:47], v[180:183], v[92:95], v[32:47]
	ds_read_b128 v[0:3], v114 offset:224
	v_mfma_f32_32x32x16_f16 v[32:47], v[184:187], v[88:91], v[32:47]
	v_mfma_f32_32x32x16_f16 v[32:47], v[188:191], v[84:87], v[32:47]
	v_mfma_f32_32x32x16_f16 v[32:47], v[192:195], v[80:83], v[32:47]
	v_mfma_f32_32x32x16_f16 v[32:47], v[196:199], v[76:79], v[32:47]
	v_mfma_f32_32x32x16_f16 v[32:47], v[200:203], v[72:75], v[32:47]
	v_mfma_f32_32x32x16_f16 v[32:47], v[204:207], v[68:71], v[32:47]
	v_mfma_f32_32x32x16_f16 v[32:47], v[208:211], v[64:67], v[32:47]
	s_waitcnt lgkmcnt(0)
	v_dot2c_f32_f16_e32 v98, v92, v8
	v_mfma_f32_32x32x16_f16 v[16:31], v[148:151], v[92:95], v[16:31]
	v_dot2c_f32_f16_e32 v98, v93, v9
	v_dot2c_f32_f16_e32 v98, v94, v10
	v_dot2c_f32_f16_e32 v98, v95, v11
	v_dot2c_f32_f16_e32 v98, v88, v12
	v_mfma_f32_32x32x16_f16 v[16:31], v[152:155], v[88:91], v[16:31]
	v_dot2c_f32_f16_e32 v98, v89, v13
	v_dot2c_f32_f16_e32 v98, v90, v14
	v_dot2c_f32_f16_e32 v98, v91, v15
	v_dot2c_f32_f16_e32 v98, v84, v234
	v_mfma_f32_32x32x16_f16 v[16:31], v[156:159], v[84:87], v[16:31]
	v_dot2c_f32_f16_e32 v98, v85, v235
	v_dot2c_f32_f16_e32 v98, v86, v236
	v_dot2c_f32_f16_e32 v98, v87, v237
	v_dot2c_f32_f16_e32 v98, v80, v238
	v_mfma_f32_32x32x16_f16 v[16:31], v[160:163], v[80:83], v[16:31]
	v_dot2c_f32_f16_e32 v98, v81, v239
	v_dot2c_f32_f16_e32 v98, v82, v240
	v_dot2c_f32_f16_e32 v98, v83, v241
	v_dot2c_f32_f16_e32 v98, v76, v242
	v_mfma_f32_32x32x16_f16 v[16:31], v[164:167], v[76:79], v[16:31]
	v_dot2c_f32_f16_e32 v98, v77, v243
	v_dot2c_f32_f16_e32 v98, v78, v244
	v_dot2c_f32_f16_e32 v98, v79, v245
	v_dot2c_f32_f16_e32 v98, v72, v106
	v_mfma_f32_32x32x16_f16 v[16:31], v[168:171], v[72:75], v[16:31]
	v_dot2c_f32_f16_e32 v98, v73, v107
	v_dot2c_f32_f16_e32 v98, v74, v108
	v_dot2c_f32_f16_e32 v98, v75, v109
	v_dot2c_f32_f16_e32 v98, v68, v110
	v_mfma_f32_32x32x16_f16 v[16:31], v[172:175], v[68:71], v[16:31]
	v_dot2c_f32_f16_e32 v98, v69, v111
	v_dot2c_f32_f16_e32 v98, v70, v112
	v_dot2c_f32_f16_e32 v98, v71, v113
	v_cvt_pk_f16_f32 v7, v38, v39
	v_cvt_pk_f16_f32 v6, v36, v37
	v_cvt_pk_f16_f32 v5, v34, v35
	v_cvt_pk_f16_f32 v4, v32, v33
	v_dot2c_f32_f16_e32 v98, v64, v0
	v_dot2c_f32_f16_e32 v98, v65, v1
	v_dot2c_f32_f16_e32 v98, v66, v2
	v_mfma_f32_32x32x16_f16 v[16:31], v[176:179], v[64:67], v[16:31]
	v_dot2c_f32_f16_e32 v98, v67, v3
	v_cvt_pk_f16_f32 v35, v46, v47
	v_cvt_pk_f16_f32 v34, v44, v45
	v_cvt_pk_f16_f32 v33, v42, v43
	v_cvt_pk_f16_f32 v32, v40, v41
	ds_bpermute_b32 v36, v102, v98
	v_cvt_f32_i32_e32 v37, v226
	v_mfma_f32_32x32x16_f16 v[0:15], v[4:7], v[60:63], 0
	s_nop 3
	v_cvt_pk_f16_f32 v23, v22, v23
	v_cvt_pk_f16_f32 v22, v20, v21
	v_cvt_pk_f16_f32 v21, v18, v19
	v_cvt_pk_f16_f32 v20, v16, v17
	v_cvt_pk_f16_f32 v19, v30, v31
	v_cvt_pk_f16_f32 v18, v28, v29
	v_cvt_pk_f16_f32 v17, v26, v27
	v_mfma_f32_32x32x16_f16 v[0:15], v[32:35], v[56:59], v[0:15]
	v_cvt_pk_f16_f32 v16, v24, v25
	s_waitcnt lgkmcnt(0)
	v_add_f32_e32 v36, v98, v36
	v_cvt_f16_f32_e32 v26, v100
	v_mov_b32_e32 v98, v97
	v_lshlrev_b32_e32 v32, 4, v218
	v_mfma_f32_32x32x16_f16 v[0:15], v[20:23], v[52:55], v[0:15]
	v_fma_mixlo_f16 v20, v37, v104, v36
	v_pack_b32_f16 v20, v20, 0
	v_pack_b32_f16 v21, v26, 0
	v_cndmask_b32_e32 v96, 0, v21, vcc
	v_mfma_f32_32x32x16_f16 v[0:15], v[16:19], v[48:51], v[0:15]
	v_cndmask_b32_e32 v16, 0, v20, vcc
	v_mov_b32_e32 v17, v97
	v_mov_b32_e32 v18, v97
	v_mov_b32_e32 v19, v97
	v_cmp_ne_u32_e32 vcc, 0, v225
	s_nop 0
	v_mfma_f32_32x32x16_f16 v[0:15], v[16:19], v[96:99], v[0:15]
	v_lshlrev_b32_e32 v70, 2, v215
	v_lshl_add_u32 v70, v214, 4, v70
	global_load_dwordx4 v[16:19], v70, s[64:65]
	global_load_dwordx4 v[20:23], v70, s[64:65] offset:32
	global_load_dwordx4 v[24:27], v70, s[64:65] offset:64
	global_load_dwordx4 v[28:31], v70, s[64:65] offset:96
	s_and_saveexec_b64 s[6:7], vcc
	s_cbranch_execz .LBB0_39
	v_lshl_or_b32 v71, v251, 12, v32
	v_add_u32_e32 v71, 0x18800, v71
	s_nop 7
	ds_write_b128 v71, v[0:3]
	ds_write_b128 v71, v[4:7] offset:1024
	ds_write_b128 v71, v[8:11] offset:2048
	ds_write_b128 v71, v[12:15] offset:3072
